# MoE routing counters spread to one 128B line each (router atomics were serializing on two cache lines)
# speedup vs baseline: 1.2904x; 1.2904x over previous
; __device__ __forceinline__ void phase_norm2(KArgs args, const bf16* H, int L, LAS unsigned char* lds, int G, int bid, int tid, int wave, int lane) {
;     ...
;     gu32* cnt = (gu32*)(ws + WS_CTL) + CW_CNT + L * 64;
;     int* ltok = (int*)(ws + WS_LTOK); float* lgate = (float*)(ws + WS_LGATE); float* lrs = (float*)(ws + WS_LRS);
;     const float* bgr = args->in[I_BGR] + L * 4; const float* ber = args->in[I_BER] + L * 32;
;     const int gw = bid * NWAVES + wave, NGW = G * NWAVES, fr = lane & 15, fq = lane >> 4;
;     const int arow[3] = {8 * (fr >> 2) + (fr & 3), 8 * (fr >> 2) + (fr & 3) + 4, 32 + (fr & 3)};
.LBB0_770:
	s_or_b64 exec, exec, s[0:1]
	s_lshl_b32 s0, s6, 3
	s_add_i32 s19, s0, s69
	s_cmpk_gt_i32 s19, 0xfff
	s_waitcnt lgkmcnt(0)
	s_barrier
	s_cbranch_scc1 .LBB0_805
	v_readlane_b32 s13, v255, 0
	s_lshl_b32 s72, s13, 6
	s_lshl_b64 s[0:1], s[72:73], 7
	s_add_u32 s0, s4, s0
	s_addc_u32 s1, s5, s1
	s_add_u32 s0, s0, 0x10000
	s_addc_u32 s1, s1, 0
	s_add_u32 s2, s4, 0x1100000
	s_addc_u32 s3, s5, 0
	s_add_u32 s6, s4, 0x2100000
	s_load_dwordx2 s[14:15], s[10:11], 0xd0
	s_load_dwordx2 s[22:23], s[10:11], 0xe0
	s_addc_u32 s7, s5, 0
	s_add_u32 s8, s4, 0x4c200000
	s_addc_u32 s9, s5, 0
	s_lshl_b32 s72, s13, 2
	s_lshl_b64 s[16:17], s[72:73], 2
	s_waitcnt lgkmcnt(0)
	s_add_u32 s10, s14, s16
	s_addc_u32 s11, s15, s17
	s_lshl_b32 s20, s12, 3
	s_bitcmp0_b32 s13, 0
	s_cselect_b32 s12, s78, 0x20100000
	s_add_u32 s4, s4, s12
	s_addc_u32 s5, s5, 0
	s_lshl_b32 s72, s13, 5
	v_lshlrev_b32_e32 v3, 1, v2
	s_waitcnt vmcnt(0)
	v_and_b32_e32 v5, 3, v2
	s_lshl_b64 s[12:13], s[72:73], 2
	v_and_b32_e32 v4, 63, v2
	v_and_b32_e32 v1, 15, v2
	v_bfe_u32 v90, v2, 4, 2
	v_and_or_b32 v6, v3, 24, v5
	s_add_u32 s12, s22, s12
	v_and_b32_e32 v2, 48, v2
	v_mov_b32_e32 v3, v0
	s_addc_u32 s13, s23, s13
	v_lshl_add_u64 v[78:79], s[4:5], 0, v[2:3]
	s_add_i32 s4, 0, 0x12240
	v_add_u32_e32 v92, 0, v2
	v_add_u32_e32 v93, s4, v2
	v_lshlrev_b32_e32 v2, 2, v4
	v_xor_b32_e32 v94, 64, v2
	v_xor_b32_e32 v95, 0x80, v2
	v_mov_b32_e32 v2, 0x10200
	v_lshlrev_b32_e32 v91, 3, v90
	v_mad_u32_u24 v97, v5, s76, v2
	v_lshlrev_b32_e32 v2, 5, v90
	v_mul_u32_u24_e32 v96, 0x810, v6
	v_lshl_add_u64 v[80:81], s[12:13], 0, v[2:3]
	v_or_b32_e32 v98, 32, v91
	s_branch .LBB0_775

; __device__ __forceinline__ void phase_norm2(KArgs args, const bf16* H, int L, LAS unsigned char* lds, int G, int bid, int tid, int wave, int lane) {
;     ...
;         if (fq == gi) {
;             float den = 0.f;
; #pragma unroll
;             for (int j = 0; j < 4; ++j) den += expf(gl[j] - gmax);
;             const float pg = 1.f / den;
;             float b1 = -3.0e38f, b2 = -3.0e38f; int j1 = 0, j2 = 0;
; #pragma unroll
;             for (int e = 0; e < 8; ++e) { const float x = (e < 4 ? acc[0][e & 3] : acc[1][e & 3]) * rstd + ber[gi * 8 + e];
;                 if (x > b1) { b2 = b1; j2 = j1; b1 = x; j1 = e; } else if (x > b2) { b2 = x; j2 = e; } }
;             const float w1 = 1.f / (1.f + expf(b2 - b1)), w2 = 1.f - w1;
;             const int s0 = gi * 8 + j1, s1 = 32 + gi * 8 + j2;
;             const unsigned r0 = __hip_atomic_fetch_add(cnt + s0, 1u, RLX_AGENT), r1 = __hip_atomic_fetch_add(cnt + s1, 1u, RLX_AGENT);
;             ltok[(size_t)s0 * NTOK + r0] = tok; lgate[(size_t)s0 * NTOK + r0] = pg * w1; lrs[(size_t)s0 * NTOK + r0] = rstd;
;             ltok[(size_t)s1 * NTOK + r1] = tok; lgate[(size_t)s1 * NTOK + r1] = pg * w2; lrs[(size_t)s1 * NTOK + r1] = rstd;
.LBB0_773:
	s_or_b64 exec, exec, s[14:15]
	v_cndmask_b32_e32 v5, v15, v17, vcc
	v_sub_f32_e32 v7, v10, v5
	v_mul_f32_e32 v8, 0x3fb8aa3b, v7
	v_fma_f32 v9, v7, s89, -v8
	v_rndne_f32_e32 v10, v8
	v_fmac_f32_e32 v9, 0x32a5705f, v7
	v_sub_f32_e32 v8, v8, v10
	v_add_f32_e32 v8, v8, v9
	v_exp_f32_e32 v8, v8
	v_cvt_i32_f32_e32 v9, v10
	s_mov_b32 s14, 0xc2ce8ed0
	v_cmp_ngt_f32_e32 vcc, s14, v7
	s_mov_b32 s15, 0x42b17218
	v_ldexp_f32 v8, v8, v9
	v_cndmask_b32_e32 v8, 0, v8, vcc
	v_cmp_nlt_f32_e32 vcc, s15, v7
	v_sub_f32_e32 v3, v3, v6
	v_mul_f32_e32 v6, 0x3fb8aa3b, v3
	v_cndmask_b32_e32 v7, v217, v8, vcc
	v_sub_f32_e32 v8, v11, v5
	v_mul_f32_e32 v9, 0x3fb8aa3b, v8
	v_fma_f32 v10, v8, s89, -v9
	v_rndne_f32_e32 v11, v9
	v_fmac_f32_e32 v10, 0x32a5705f, v8
	v_sub_f32_e32 v9, v9, v11
	v_add_f32_e32 v9, v9, v10
	v_exp_f32_e32 v9, v9
	v_cvt_i32_f32_e32 v10, v11
	v_cmp_ngt_f32_e32 vcc, s14, v8
	v_ldexp_f32 v9, v9, v10
	s_nop 0
	v_cndmask_b32_e32 v9, 0, v9, vcc
	v_cmp_nlt_f32_e32 vcc, s15, v8
	s_nop 1
	v_cndmask_b32_e32 v8, v217, v9, vcc
	v_add_f32_e32 v7, v7, v8
	v_sub_f32_e32 v8, v14, v5
	v_mul_f32_e32 v9, 0x3fb8aa3b, v8
	v_fma_f32 v10, v8, s89, -v9
	v_rndne_f32_e32 v11, v9
	v_fmac_f32_e32 v10, 0x32a5705f, v8
	v_sub_f32_e32 v9, v9, v11
	v_add_f32_e32 v9, v9, v10
	v_exp_f32_e32 v9, v9
	v_cvt_i32_f32_e32 v10, v11
	v_cmp_ngt_f32_e32 vcc, s14, v8
	v_sub_f32_e32 v5, v17, v5
	v_ldexp_f32 v9, v9, v10
	v_cndmask_b32_e32 v9, 0, v9, vcc
	v_cmp_nlt_f32_e32 vcc, s15, v8
	s_nop 1
	v_cndmask_b32_e32 v8, v217, v9, vcc
	v_add_f32_e32 v7, v8, v7
	v_mul_f32_e32 v8, 0x3fb8aa3b, v5
	v_fma_f32 v9, v5, s89, -v8
	v_rndne_f32_e32 v10, v8
	v_fmac_f32_e32 v9, 0x32a5705f, v5
	v_sub_f32_e32 v8, v8, v10
	v_add_f32_e32 v8, v8, v9
	v_exp_f32_e32 v8, v8
	v_cvt_i32_f32_e32 v9, v10
	v_cmp_ngt_f32_e32 vcc, s14, v5
	v_ldexp_f32 v8, v8, v9
	s_nop 0
	v_cndmask_b32_e32 v8, 0, v8, vcc
	v_cmp_nlt_f32_e32 vcc, s15, v5
	s_nop 1
	v_cndmask_b32_e32 v5, v217, v8, vcc
	v_add_f32_e32 v5, v5, v7
	v_div_scale_f32 v7, s[4:5], v5, v5, 1.0
	v_rcp_f32_e32 v8, v7
	s_nop 0
	v_fma_f32 v9, -v7, v8, 1.0
	v_fmac_f32_e32 v8, v9, v8
	v_div_scale_f32 v9, vcc, 1.0, v5, 1.0
	v_mul_f32_e32 v10, v9, v8
	v_fma_f32 v11, -v7, v10, v9
	v_fmac_f32_e32 v10, v11, v8
	v_fma_f32 v7, -v7, v10, v9
	v_div_fmas_f32 v7, v7, v8, v10
	v_div_fixup_f32 v5, v7, v5, 1.0
	v_fma_f32 v7, v3, s89, -v6
	v_rndne_f32_e32 v8, v6
	v_fmac_f32_e32 v7, 0x32a5705f, v3
	v_sub_f32_e32 v6, v6, v8
	v_add_f32_e32 v6, v6, v7
	v_exp_f32_e32 v6, v6
	v_cvt_i32_f32_e32 v7, v8
	v_cmp_ngt_f32_e32 vcc, s14, v3
	v_mov_b32_e32 v11, v0
	v_ldexp_f32 v6, v6, v7
	v_cndmask_b32_e32 v6, 0, v6, vcc
	v_cmp_nlt_f32_e32 vcc, s15, v3
	s_nop 1
	v_cndmask_b32_e32 v3, v217, v6, vcc
	v_add_f32_e32 v3, 1.0, v3
	v_div_scale_f32 v6, s[4:5], v3, v3, 1.0
	v_rcp_f32_e32 v7, v6
	s_nop 0
	v_fma_f32 v8, -v6, v7, 1.0
	v_fmac_f32_e32 v7, v8, v7
	v_div_scale_f32 v8, vcc, 1.0, v3, 1.0
	v_mul_f32_e32 v9, v8, v7
	v_fma_f32 v10, -v6, v9, v8
	v_fmac_f32_e32 v9, v10, v7
	v_fma_f32 v6, -v6, v9, v8
	v_div_fmas_f32 v6, v6, v7, v9
	v_div_fixup_f32 v7, v6, v3, 1.0
	v_add_u32_e32 v3, v2, v91
	v_lshlrev_b32_e32 v2, 7, v3
	global_atomic_add v2, v2, v207, s[0:1] sc0
	v_add_lshl_u32 v8, v91, v4, 7
	v_add_u32_e32 v8, 0x1000, v8
	global_atomic_add v8, v8, v207, s[0:1] sc0
	v_lshlrev_b32_e32 v10, 16, v3
	v_mov_b32_e32 v3, v0
	v_mov_b32_e32 v9, v0
	v_sub_f32_e32 v6, 1.0, v7
	v_mul_f32_e32 v7, v5, v7
	v_mul_f32_e32 v6, v5, v6
	s_waitcnt vmcnt(1)
	v_lshl_add_u64 v[2:3], v[10:11], 0, v[2:3]
	v_lshlrev_b64 v[2:3], 2, v[2:3]
	v_lshl_add_u64 v[10:11], s[2:3], 0, v[2:3]
	global_store_dword v[10:11], v82, off
	v_lshl_add_u64 v[10:11], s[6:7], 0, v[2:3]
	v_lshl_add_u64 v[2:3], s[8:9], 0, v[2:3]
	global_store_dword v[2:3], v18, off
	v_add_lshl_u32 v2, v98, v4, 16
	v_mov_b32_e32 v3, v0
	s_waitcnt vmcnt(2)
	v_lshl_add_u64 v[2:3], v[2:3], 0, v[8:9]
	v_lshlrev_b64 v[2:3], 2, v[2:3]
	v_lshl_add_u64 v[8:9], s[2:3], 0, v[2:3]
	v_lshl_add_u64 v[4:5], s[6:7], 0, v[2:3]
	v_lshl_add_u64 v[2:3], s[8:9], 0, v[2:3]
	global_store_dword v[10:11], v7, off
	global_store_dword v[8:9], v82, off
	global_store_dword v[4:5], v6, off
	global_store_dword v[2:3], v18, off

; #define LAS __attribute__((address_space(3)))
; __global__ void __launch_bounds__(NWAVES * 64, 2) fwd_kernel(Args args) {
;     ...
;             LAS int* tab = (LAS int*)(lds + TAB_OFF);
;             { PHASE_IDS
;             __syncthreads();
;             if (tid < 64) { const int c = (int)__hip_atomic_load((gu32*)(ws + WS_CTL) + CW_CNT + L * 64 + tid, RLX_AGENT); tab[80 + tid] = c; tab[160 + tid] = (c + 255) >> 8; }
;             __syncthreads();
.LBB0_863:
	s_and_b64 vcc, exec, s[0:1]
	s_cbranch_vccz .LBB0_1094
	s_mov_b64 s[2:3], s[66:67]
	s_mov_b32 s0, s65
	s_mov_b32 s1, s68
	v_mbcnt_lo_u32_b32 v1, -1, 0
	v_mbcnt_hi_u32_b32 v1, -1, v1
	s_nop 0
	v_add_u32_e32 v2, s70, v1
	s_nop 0
	v_cmp_gt_i32_e32 vcc, 64, v2
	s_barrier
	s_and_saveexec_b64 s[0:1], vcc
	s_cbranch_execz .LBB0_866
	s_load_dwordx2 s[2:3], s[2:3], 0x130
	v_readlane_b32 s4, v255, 0
	s_lshl_b32 s72, s4, 6
	s_lshl_b64 s[4:5], s[72:73], 7
	v_ashrrev_i32_e32 v3, 31, v2
	s_waitcnt lgkmcnt(0)
	s_add_u32 s2, s2, s4
	s_addc_u32 s3, s3, s5
	s_waitcnt vmcnt(0)
	v_lshlrev_b32_e32 v6, 5, v2
	v_mov_b32_e32 v7, 0
	v_lshl_add_u64 v[4:5], v[6:7], 2, s[2:3]
	v_add_co_u32_e32 v4, vcc, 0x10000, v4
	v_readlane_b32 s2, v254, 16
	s_nop 0
	v_addc_co_u32_e32 v5, vcc, 0, v5, vcc
	global_load_dword v1, v[4:5], off sc1
	v_lshl_add_u32 v3, v2, 2, s2
	s_waitcnt vmcnt(0)
	v_add_u32_e32 v4, 0xff, v1
	v_ashrrev_i32_e32 v4, 8, v4
	ds_write2_b32 v3, v1, v4 offset0:80 offset1:160
